# attention QK^T: software-pipelined K-fragment LDS reads in the three flash loops (8 buffers in free VGPRs)
# speedup vs baseline: 1.0124x; 1.0124x over previous
; #define LAS __attribute__((address_space(3)))
; #define SBAR() __builtin_amdgcn_sched_barrier(0)
; template <int OFF> __device__ __forceinline__ s16x4 tr_read(int vb) { s16x4 r; asm volatile("ds_read_b64_tr_b16 %0, %1 offset:%2" : "=&v"(r) : "v"(vb), "i"(OFF) : "memory"); return r; }
; __device__ __forceinline__ void qkt(f32x16& p0, f32x16& p1, const LAS char* Ks, const bf16x8 (&qr)[8], int r32, int hi) {
;     p0 = f32x16{}; p1 = f32x16{};
; #pragma unroll
;     for (int d0 = 0; d0 < 8; ++d0) { const int cb = (d0 * 16 + hi * 8) * 2;
;         const bf16x8 b0 = *(const LAS bf16x8*)(Ks + KSWZ(r32, cb));
;         const bf16x8 b1 = *(const LAS bf16x8*)(Ks + KSWZ(32 + r32, cb));
;         p0 = __builtin_amdgcn_mfma_f32_32x32x16_bf16(b0, qr[d0], p0, 0, 0, 0);
;         p1 = __builtin_amdgcn_mfma_f32_32x32x16_bf16(b1, qr[d0], p1, 0, 0, 0);
;         if (d0 == 3) SBAR(); }
; }
; template <int D0> __device__ __forceinline__ void pv_one(f32x16& od, int vb, bf16x8 pa0, bf16x8 pa1, bf16x8 pa2, bf16x8 pa3) {
;     const s16x4 l0 = tr_read<v_rd_off(D0, 0, 0)>(vb), h0 = tr_read<v_rd_off(D0, 0, 1)>(vb), l1 = tr_read<v_rd_off(D0, 1, 0)>(vb), h1 = tr_read<v_rd_off(D0, 1, 1)>(vb);
;     const s16x4 l2 = tr_read<v_rd_off(D0, 2, 0)>(vb), h2 = tr_read<v_rd_off(D0, 2, 1)>(vb), l3 = tr_read<v_rd_off(D0, 3, 0)>(vb), h3 = tr_read<v_rd_off(D0, 3, 1)>(vb);
;     asm volatile("s_waitcnt lgkmcnt(0)" ::: "memory"); SBAR();
;     ...
;     od = __builtin_amdgcn_mfma_f32_32x32x16_bf16(pa0, PK(l0, h0), od, 0, 0, 0);
;     od = __builtin_amdgcn_mfma_f32_32x32x16_bf16(pa1, PK(l1, h1), od, 0, 0, 0);
;     od = __builtin_amdgcn_mfma_f32_32x32x16_bf16(pa2, PK(l2, h2), od, 0, 0, 0);
;     od = __builtin_amdgcn_mfma_f32_32x32x16_bf16(pa3, PK(l3, h3), od, 0, 0, 0);
;     ...
; }
.LBB0_599:
	s_lshl_b32 s29, s17, 14
	s_add_i32 s34, s29, 0xffffc000
	s_cmp_lg_u32 s17, 0
	s_cselect_b32 s17, s34, 0x8000
	v_add_u32_e32 v144, s17, v165
	ds_read_b64_tr_b16 v[84:85], v144 offset:0
	ds_read_b64_tr_b16 v[86:87], v144 offset:0x800
	ds_read_b64_tr_b16 v[88:89], v144 offset:0x1000
	ds_read_b64_tr_b16 v[90:91], v144 offset:0x1800
	ds_read_b64_tr_b16 v[92:93], v144 offset:0x2000
	ds_read_b64_tr_b16 v[94:95], v144 offset:0x2800
	ds_read_b64_tr_b16 v[96:97], v144 offset:0x3000
	ds_read_b64_tr_b16 v[98:99], v144 offset:0x3800
	s_waitcnt lgkmcnt(0)
	s_nop 0
	v_mfma_f32_32x32x16_bf16 v[20:35], v[72:75], v[84:87], v[20:35]
	ds_read_b64_tr_b16 v[84:85], v144 offset:0x200
	ds_read_b64_tr_b16 v[86:87], v144 offset:0xa00
	v_add_u32_e32 v246, s29, v148
	v_add_u32_e32 v247, v246, v149
	ds_read_b128 v[212:215], v247 offset:49152
	v_mfma_f32_32x32x16_bf16 v[20:35], v[76:79], v[88:91], v[20:35]
	ds_read_b64_tr_b16 v[88:89], v144 offset:0x1200
	ds_read_b64_tr_b16 v[90:91], v144 offset:0x1a00
	ds_read_b128 v[216:219], v247 offset:57344
	v_mfma_f32_32x32x16_bf16 v[20:35], v[80:83], v[92:95], v[20:35]
	ds_read_b64_tr_b16 v[92:93], v144 offset:0x2200
	ds_read_b64_tr_b16 v[94:95], v144 offset:0x2a00
	v_add_u32_e32 v247, v246, v150
	ds_read_b128 v[220:223], v247 offset:49152
	v_mfma_f32_32x32x16_bf16 v[20:35], v[68:71], v[96:99], v[20:35]
	ds_read_b64_tr_b16 v[96:97], v144 offset:0x3200
	ds_read_b64_tr_b16 v[98:99], v144 offset:0x3a00
	ds_read_b128 v[224:227], v247 offset:57344
	s_waitcnt lgkmcnt(0)
	v_mfma_f32_32x32x16_bf16 v[36:51], v[72:75], v[84:87], v[36:51]
	ds_read_b64_tr_b16 v[84:85], v144 offset:0x400
	ds_read_b64_tr_b16 v[86:87], v144 offset:0xc00
	v_add_u32_e32 v247, v246, v151
	ds_read_b128 v[228:231], v247 offset:49152
	v_mfma_f32_32x32x16_bf16 v[36:51], v[76:79], v[88:91], v[36:51]
	ds_read_b64_tr_b16 v[88:89], v144 offset:0x1400
	ds_read_b64_tr_b16 v[90:91], v144 offset:0x1c00
	ds_read_b128 v[232:235], v247 offset:57344
	v_mfma_f32_32x32x16_bf16 v[36:51], v[80:83], v[92:95], v[36:51]
	ds_read_b64_tr_b16 v[92:93], v144 offset:0x2400
	ds_read_b64_tr_b16 v[94:95], v144 offset:0x2c00
	v_add_u32_e32 v247, v246, v167
	ds_read_b128 v[236:239], v247 offset:49152
	v_mfma_f32_32x32x16_bf16 v[36:51], v[68:71], v[96:99], v[36:51]
	ds_read_b64_tr_b16 v[96:97], v144 offset:0x3400
	ds_read_b64_tr_b16 v[98:99], v144 offset:0x3c00
	ds_read_b128 v[240:243], v247 offset:57344
	s_waitcnt lgkmcnt(0)
	v_mfma_f32_32x32x16_bf16 v[52:67], v[72:75], v[84:87], v[52:67]
	ds_read_b64_tr_b16 v[84:85], v144 offset:0x600
	ds_read_b64_tr_b16 v[86:87], v144 offset:0xe00
	v_mfma_f32_32x32x16_bf16 v[52:67], v[76:79], v[88:91], v[52:67]
	ds_read_b64_tr_b16 v[88:89], v144 offset:0x1600
	ds_read_b64_tr_b16 v[90:91], v144 offset:0x1e00
	v_mfma_f32_32x32x16_bf16 v[52:67], v[80:83], v[92:95], v[52:67]
	ds_read_b64_tr_b16 v[92:93], v144 offset:0x2600
	ds_read_b64_tr_b16 v[94:95], v144 offset:0x2e00
	v_mfma_f32_32x32x16_bf16 v[52:67], v[68:71], v[96:99], v[52:67]
	ds_read_b64_tr_b16 v[96:97], v144 offset:0x3600
	ds_read_b64_tr_b16 v[98:99], v144 offset:0x3e00
	s_waitcnt lgkmcnt(0)
	v_mfma_f32_32x32x16_bf16 v[4:19], v[72:75], v[84:87], v[4:19]
	v_mfma_f32_32x32x16_bf16 v[4:19], v[76:79], v[88:91], v[4:19]
	v_mfma_f32_32x32x16_bf16 v[4:19], v[80:83], v[92:95], v[4:19]
	v_mfma_f32_32x32x16_bf16 v[4:19], v[68:71], v[96:99], v[4:19]
	s_and_b64 vcc, exec, s[12:13]
	v_mfma_f32_32x32x16_bf16 v[68:83], v[212:215], v[124:127], 0
	v_add_u32_e32 v247, v246, v169
	ds_read_b128 v[212:215], v247 offset:49152
	v_mfma_f32_32x32x16_bf16 v[84:99], v[216:219], v[124:127], 0
	ds_read_b128 v[216:219], v247 offset:57344
	v_mfma_f32_32x32x16_bf16 v[68:83], v[220:223], v[100:103], v[68:83]
	v_add_u32_e32 v247, v246, v176
	ds_read_b128 v[220:223], v247 offset:49152
	v_mfma_f32_32x32x16_bf16 v[84:99], v[224:227], v[100:103], v[84:99]
	ds_read_b128 v[224:227], v247 offset:57344
	v_mfma_f32_32x32x16_bf16 v[68:83], v[228:231], v[104:107], v[68:83]
	v_add_u32_e32 v247, v246, v177
	ds_read_b128 v[228:231], v247 offset:49152
	v_mfma_f32_32x32x16_bf16 v[84:99], v[232:235], v[104:107], v[84:99]
	ds_read_b128 v[232:235], v247 offset:57344
	v_mfma_f32_32x32x16_bf16 v[68:83], v[236:239], v[108:111], v[68:83]
	v_add_u32_e32 v247, v246, v178
	ds_read_b128 v[236:239], v247 offset:49152
	v_mfma_f32_32x32x16_bf16 v[84:99], v[240:243], v[108:111], v[84:99]
	ds_read_b128 v[240:243], v247 offset:57344
	s_waitcnt lgkmcnt(7)
	v_mfma_f32_32x32x16_bf16 v[68:83], v[212:215], v[112:115], v[68:83]
	s_waitcnt lgkmcnt(6)
	v_mfma_f32_32x32x16_bf16 v[84:99], v[216:219], v[112:115], v[84:99]
	s_waitcnt lgkmcnt(5)
	v_mfma_f32_32x32x16_bf16 v[68:83], v[220:223], v[116:119], v[68:83]
	s_waitcnt lgkmcnt(4)
	v_mfma_f32_32x32x16_bf16 v[84:99], v[224:227], v[116:119], v[84:99]
	s_waitcnt lgkmcnt(3)
	v_mfma_f32_32x32x16_bf16 v[68:83], v[228:231], v[120:123], v[68:83]
	s_waitcnt lgkmcnt(2)
	v_mfma_f32_32x32x16_bf16 v[84:99], v[232:235], v[120:123], v[84:99]
	s_waitcnt lgkmcnt(1)
	v_mfma_f32_32x32x16_bf16 v[68:83], v[236:239], v[128:131], v[68:83]
	s_waitcnt lgkmcnt(0)
	v_mfma_f32_32x32x16_bf16 v[84:99], v[240:243], v[128:131], v[84:99]
	s_cbranch_vccnz .LBB0_601
	s_waitcnt vmcnt(0)

; #define LAS __attribute__((address_space(3)))
; #define SBAR() __builtin_amdgcn_sched_barrier(0)
; template <int OFF> __device__ __forceinline__ s16x4 tr_read(int vb) { s16x4 r; asm volatile("ds_read_b64_tr_b16 %0, %1 offset:%2" : "=&v"(r) : "v"(vb), "i"(OFF) : "memory"); return r; }
; __device__ __forceinline__ void qkt(f32x16& p0, f32x16& p1, const LAS char* Ks, const bf16x8 (&qr)[8], int r32, int hi) {
;     p0 = f32x16{}; p1 = f32x16{};
; #pragma unroll
;     for (int d0 = 0; d0 < 8; ++d0) { const int cb = (d0 * 16 + hi * 8) * 2;
;         const bf16x8 b0 = *(const LAS bf16x8*)(Ks + KSWZ(r32, cb));
;         const bf16x8 b1 = *(const LAS bf16x8*)(Ks + KSWZ(32 + r32, cb));
;         p0 = __builtin_amdgcn_mfma_f32_32x32x16_bf16(b0, qr[d0], p0, 0, 0, 0);
;         p1 = __builtin_amdgcn_mfma_f32_32x32x16_bf16(b1, qr[d0], p1, 0, 0, 0);
;         if (d0 == 3) SBAR(); }
; }
; template <int D0> __device__ __forceinline__ void pv_one(f32x16& od, int vb, bf16x8 pa0, bf16x8 pa1, bf16x8 pa2, bf16x8 pa3) {
;     const s16x4 l0 = tr_read<v_rd_off(D0, 0, 0)>(vb), h0 = tr_read<v_rd_off(D0, 0, 1)>(vb), l1 = tr_read<v_rd_off(D0, 1, 0)>(vb), h1 = tr_read<v_rd_off(D0, 1, 1)>(vb);
;     const s16x4 l2 = tr_read<v_rd_off(D0, 2, 0)>(vb), h2 = tr_read<v_rd_off(D0, 2, 1)>(vb), l3 = tr_read<v_rd_off(D0, 3, 0)>(vb), h3 = tr_read<v_rd_off(D0, 3, 1)>(vb);
;     asm volatile("s_waitcnt lgkmcnt(0)" ::: "memory"); SBAR();
;     ...
;     od = __builtin_amdgcn_mfma_f32_32x32x16_bf16(pa0, PK(l0, h0), od, 0, 0, 0);
;     od = __builtin_amdgcn_mfma_f32_32x32x16_bf16(pa1, PK(l1, h1), od, 0, 0, 0);
;     od = __builtin_amdgcn_mfma_f32_32x32x16_bf16(pa2, PK(l2, h2), od, 0, 0, 0);
;     od = __builtin_amdgcn_mfma_f32_32x32x16_bf16(pa3, PK(l3, h3), od, 0, 0, 0);
;     ...
; }
.LBB0_775:
	s_lshl_b32 s18, s13, 14
	s_add_i32 s19, s18, 0xffffc000
	s_cmp_lg_u32 s13, 0
	s_cselect_b32 s13, s19, 0x8000
	v_add_u32_e32 v188, s13, v165
	ds_read_b64_tr_b16 v[84:85], v188 offset:0
	ds_read_b64_tr_b16 v[86:87], v188 offset:0x800
	ds_read_b64_tr_b16 v[88:89], v188 offset:0x1000
	ds_read_b64_tr_b16 v[90:91], v188 offset:0x1800
	ds_read_b64_tr_b16 v[92:93], v188 offset:0x2000
	ds_read_b64_tr_b16 v[94:95], v188 offset:0x2800
	ds_read_b64_tr_b16 v[96:97], v188 offset:0x3000
	ds_read_b64_tr_b16 v[98:99], v188 offset:0x3800
	s_waitcnt lgkmcnt(0)
	s_nop 0
	v_mfma_f32_32x32x16_bf16 v[20:35], v[72:75], v[84:87], v[20:35]
	ds_read_b64_tr_b16 v[84:85], v188 offset:0x200
	ds_read_b64_tr_b16 v[86:87], v188 offset:0xa00
	v_add_u32_e32 v246, s18, v173
	v_add_u32_e32 v247, v246, v174
	ds_read_b128 v[212:215], v247 offset:49152
	v_mfma_f32_32x32x16_bf16 v[20:35], v[76:79], v[88:91], v[20:35]
	ds_read_b64_tr_b16 v[88:89], v188 offset:0x1200
	ds_read_b64_tr_b16 v[90:91], v188 offset:0x1a00
	ds_read_b128 v[216:219], v247 offset:57344
	v_mfma_f32_32x32x16_bf16 v[20:35], v[80:83], v[92:95], v[20:35]
	ds_read_b64_tr_b16 v[92:93], v188 offset:0x2200
	ds_read_b64_tr_b16 v[94:95], v188 offset:0x2a00
	v_add_u32_e32 v247, v246, v175
	ds_read_b128 v[220:223], v247 offset:49152
	v_mfma_f32_32x32x16_bf16 v[20:35], v[68:71], v[96:99], v[20:35]
	ds_read_b64_tr_b16 v[96:97], v188 offset:0x3200
	ds_read_b64_tr_b16 v[98:99], v188 offset:0x3a00
	ds_read_b128 v[224:227], v247 offset:57344
	s_waitcnt lgkmcnt(0)
	v_mfma_f32_32x32x16_bf16 v[36:51], v[72:75], v[84:87], v[36:51]
	ds_read_b64_tr_b16 v[84:85], v188 offset:0x400
	ds_read_b64_tr_b16 v[86:87], v188 offset:0xc00
	v_add_u32_e32 v247, v246, v176
	ds_read_b128 v[228:231], v247 offset:49152
	v_mfma_f32_32x32x16_bf16 v[36:51], v[76:79], v[88:91], v[36:51]
	ds_read_b64_tr_b16 v[88:89], v188 offset:0x1400
	ds_read_b64_tr_b16 v[90:91], v188 offset:0x1c00
	ds_read_b128 v[232:235], v247 offset:57344
	v_mfma_f32_32x32x16_bf16 v[36:51], v[80:83], v[92:95], v[36:51]
	ds_read_b64_tr_b16 v[92:93], v188 offset:0x2400
	ds_read_b64_tr_b16 v[94:95], v188 offset:0x2c00
	v_add_u32_e32 v247, v246, v177
	ds_read_b128 v[236:239], v247 offset:49152
	v_mfma_f32_32x32x16_bf16 v[36:51], v[68:71], v[96:99], v[36:51]
	ds_read_b64_tr_b16 v[96:97], v188 offset:0x3400
	ds_read_b64_tr_b16 v[98:99], v188 offset:0x3c00
	ds_read_b128 v[240:243], v247 offset:57344
	s_waitcnt lgkmcnt(0)
	v_mfma_f32_32x32x16_bf16 v[52:67], v[72:75], v[84:87], v[52:67]
	ds_read_b64_tr_b16 v[84:85], v188 offset:0x600
	ds_read_b64_tr_b16 v[86:87], v188 offset:0xe00
	v_mfma_f32_32x32x16_bf16 v[52:67], v[76:79], v[88:91], v[52:67]
	ds_read_b64_tr_b16 v[88:89], v188 offset:0x1600
	ds_read_b64_tr_b16 v[90:91], v188 offset:0x1e00
	v_mfma_f32_32x32x16_bf16 v[52:67], v[80:83], v[92:95], v[52:67]
	ds_read_b64_tr_b16 v[92:93], v188 offset:0x2600
	ds_read_b64_tr_b16 v[94:95], v188 offset:0x2e00
	v_mfma_f32_32x32x16_bf16 v[52:67], v[68:71], v[96:99], v[52:67]
	ds_read_b64_tr_b16 v[96:97], v188 offset:0x3600
	ds_read_b64_tr_b16 v[98:99], v188 offset:0x3e00
	s_waitcnt lgkmcnt(0)
	v_mfma_f32_32x32x16_bf16 v[4:19], v[72:75], v[84:87], v[4:19]
	v_mfma_f32_32x32x16_bf16 v[4:19], v[76:79], v[88:91], v[4:19]
	v_mfma_f32_32x32x16_bf16 v[4:19], v[80:83], v[92:95], v[4:19]
	v_mfma_f32_32x32x16_bf16 v[4:19], v[68:71], v[96:99], v[4:19]
	s_and_b64 vcc, exec, s[10:11]
	v_mfma_f32_32x32x16_bf16 v[68:83], v[212:215], v[124:127], 0
	v_add_u32_e32 v247, v246, v178
	ds_read_b128 v[212:215], v247 offset:49152
	v_mfma_f32_32x32x16_bf16 v[84:99], v[216:219], v[124:127], 0
	ds_read_b128 v[216:219], v247 offset:57344
	v_mfma_f32_32x32x16_bf16 v[68:83], v[220:223], v[100:103], v[68:83]
	v_add_u32_e32 v247, v246, v179
	ds_read_b128 v[220:223], v247 offset:49152
	v_mfma_f32_32x32x16_bf16 v[84:99], v[224:227], v[100:103], v[84:99]
	ds_read_b128 v[224:227], v247 offset:57344
	v_mfma_f32_32x32x16_bf16 v[68:83], v[228:231], v[104:107], v[68:83]
	v_add_u32_e32 v247, v246, v180
	ds_read_b128 v[228:231], v247 offset:49152
	v_mfma_f32_32x32x16_bf16 v[84:99], v[232:235], v[104:107], v[84:99]
	ds_read_b128 v[232:235], v247 offset:57344
	v_mfma_f32_32x32x16_bf16 v[68:83], v[236:239], v[108:111], v[68:83]
	v_add_u32_e32 v247, v246, v181
	ds_read_b128 v[236:239], v247 offset:49152
	v_mfma_f32_32x32x16_bf16 v[84:99], v[240:243], v[108:111], v[84:99]
	ds_read_b128 v[240:243], v247 offset:57344
	s_waitcnt lgkmcnt(7)
	v_mfma_f32_32x32x16_bf16 v[68:83], v[212:215], v[112:115], v[68:83]
	s_waitcnt lgkmcnt(6)
	v_mfma_f32_32x32x16_bf16 v[84:99], v[216:219], v[112:115], v[84:99]
	s_waitcnt lgkmcnt(5)
	v_mfma_f32_32x32x16_bf16 v[68:83], v[220:223], v[116:119], v[68:83]
	s_waitcnt lgkmcnt(4)
	v_mfma_f32_32x32x16_bf16 v[84:99], v[224:227], v[116:119], v[84:99]
	s_waitcnt lgkmcnt(3)
	v_mfma_f32_32x32x16_bf16 v[68:83], v[228:231], v[120:123], v[68:83]
	s_waitcnt lgkmcnt(2)
	v_mfma_f32_32x32x16_bf16 v[84:99], v[232:235], v[120:123], v[84:99]
	s_waitcnt lgkmcnt(1)
	v_mfma_f32_32x32x16_bf16 v[68:83], v[236:239], v[128:131], v[68:83]
	s_waitcnt lgkmcnt(0)
	v_mfma_f32_32x32x16_bf16 v[84:99], v[240:243], v[128:131], v[84:99]
	s_cbranch_vccnz .LBB0_777
	s_waitcnt vmcnt(0)

; #define LAS __attribute__((address_space(3)))
; #define SBAR() __builtin_amdgcn_sched_barrier(0)
; template <int OFF> __device__ __forceinline__ s16x4 tr_read(int vb) { s16x4 r; asm volatile("ds_read_b64_tr_b16 %0, %1 offset:%2" : "=&v"(r) : "v"(vb), "i"(OFF) : "memory"); return r; }
; __device__ __forceinline__ void qkt(f32x16& p0, f32x16& p1, const LAS char* Ks, const bf16x8 (&qr)[8], int r32, int hi) {
;     p0 = f32x16{}; p1 = f32x16{};
; #pragma unroll
;     for (int d0 = 0; d0 < 8; ++d0) { const int cb = (d0 * 16 + hi * 8) * 2;
;         const bf16x8 b0 = *(const LAS bf16x8*)(Ks + KSWZ(r32, cb));
;         const bf16x8 b1 = *(const LAS bf16x8*)(Ks + KSWZ(32 + r32, cb));
;         p0 = __builtin_amdgcn_mfma_f32_32x32x16_bf16(b0, qr[d0], p0, 0, 0, 0);
;         p1 = __builtin_amdgcn_mfma_f32_32x32x16_bf16(b1, qr[d0], p1, 0, 0, 0);
;         if (d0 == 3) SBAR(); }
; }
; template <int D0> __device__ __forceinline__ void pv_one(f32x16& od, int vb, bf16x8 pa0, bf16x8 pa1, bf16x8 pa2, bf16x8 pa3) {
;     const s16x4 l0 = tr_read<v_rd_off(D0, 0, 0)>(vb), h0 = tr_read<v_rd_off(D0, 0, 1)>(vb), l1 = tr_read<v_rd_off(D0, 1, 0)>(vb), h1 = tr_read<v_rd_off(D0, 1, 1)>(vb);
;     const s16x4 l2 = tr_read<v_rd_off(D0, 2, 0)>(vb), h2 = tr_read<v_rd_off(D0, 2, 1)>(vb), l3 = tr_read<v_rd_off(D0, 3, 0)>(vb), h3 = tr_read<v_rd_off(D0, 3, 1)>(vb);
;     asm volatile("s_waitcnt lgkmcnt(0)" ::: "memory"); SBAR();
;     ...
;     od = __builtin_amdgcn_mfma_f32_32x32x16_bf16(pa0, PK(l0, h0), od, 0, 0, 0);
;     od = __builtin_amdgcn_mfma_f32_32x32x16_bf16(pa1, PK(l1, h1), od, 0, 0, 0);
;     od = __builtin_amdgcn_mfma_f32_32x32x16_bf16(pa2, PK(l2, h2), od, 0, 0, 0);
;     od = __builtin_amdgcn_mfma_f32_32x32x16_bf16(pa3, PK(l3, h3), od, 0, 0, 0);
;     ...
; }
.LBB0_833:
	v_sub_co_u32_e64 v2, s[14:15], s13, 1
	s_and_b64 s[14:15], s[14:15], exec
	v_readfirstlane_b32 s14, v2
	s_cselect_b32 s14, 2, s14
	s_lshl_b32 s14, s14, 14
	v_add_u32_e32 v2, s14, v165
	ds_read_b64_tr_b16 v[84:85], v2 offset:0
	ds_read_b64_tr_b16 v[86:87], v2 offset:0x800
	ds_read_b64_tr_b16 v[88:89], v2 offset:0x1000
	ds_read_b64_tr_b16 v[90:91], v2 offset:0x1800
	ds_read_b64_tr_b16 v[92:93], v2 offset:0x2000
	ds_read_b64_tr_b16 v[94:95], v2 offset:0x2800
	ds_read_b64_tr_b16 v[96:97], v2 offset:0x3000
	ds_read_b64_tr_b16 v[98:99], v2 offset:0x3800
	s_waitcnt lgkmcnt(0)
	s_nop 0
	v_mfma_f32_32x32x16_bf16 v[20:35], v[72:75], v[84:87], v[20:35]
	ds_read_b64_tr_b16 v[84:85], v2 offset:0x200
	ds_read_b64_tr_b16 v[86:87], v2 offset:0xa00
	v_lshl_add_u32 v246, s13, 14, v170
	v_add_u32_e32 v247, v246, v171
	ds_read_b128 v[212:215], v247 offset:49152
	v_mfma_f32_32x32x16_bf16 v[20:35], v[76:79], v[88:91], v[20:35]
	ds_read_b64_tr_b16 v[88:89], v2 offset:0x1200
	ds_read_b64_tr_b16 v[90:91], v2 offset:0x1a00
	ds_read_b128 v[216:219], v247 offset:57344
	v_mfma_f32_32x32x16_bf16 v[20:35], v[80:83], v[92:95], v[20:35]
	ds_read_b64_tr_b16 v[92:93], v2 offset:0x2200
	ds_read_b64_tr_b16 v[94:95], v2 offset:0x2a00
	v_add_u32_e32 v247, v246, v172
	ds_read_b128 v[220:223], v247 offset:49152
	v_mfma_f32_32x32x16_bf16 v[20:35], v[68:71], v[96:99], v[20:35]
	ds_read_b64_tr_b16 v[96:97], v2 offset:0x3200
	ds_read_b64_tr_b16 v[98:99], v2 offset:0x3a00
	ds_read_b128 v[224:227], v247 offset:57344
	s_waitcnt lgkmcnt(0)
	v_mfma_f32_32x32x16_bf16 v[36:51], v[72:75], v[84:87], v[36:51]
	ds_read_b64_tr_b16 v[84:85], v2 offset:0x400
	ds_read_b64_tr_b16 v[86:87], v2 offset:0xc00
	v_add_u32_e32 v247, v246, v173
	ds_read_b128 v[228:231], v247 offset:49152
	v_mfma_f32_32x32x16_bf16 v[36:51], v[76:79], v[88:91], v[36:51]
	ds_read_b64_tr_b16 v[88:89], v2 offset:0x1400
	ds_read_b64_tr_b16 v[90:91], v2 offset:0x1c00
	ds_read_b128 v[232:235], v247 offset:57344
	v_mfma_f32_32x32x16_bf16 v[36:51], v[80:83], v[92:95], v[36:51]
	ds_read_b64_tr_b16 v[92:93], v2 offset:0x2400
	ds_read_b64_tr_b16 v[94:95], v2 offset:0x2c00
	v_add_u32_e32 v247, v246, v174
	ds_read_b128 v[236:239], v247 offset:49152
	v_mfma_f32_32x32x16_bf16 v[36:51], v[68:71], v[96:99], v[36:51]
	ds_read_b64_tr_b16 v[96:97], v2 offset:0x3400
	ds_read_b64_tr_b16 v[98:99], v2 offset:0x3c00
	ds_read_b128 v[240:243], v247 offset:57344
	s_waitcnt lgkmcnt(0)
	v_mfma_f32_32x32x16_bf16 v[52:67], v[72:75], v[84:87], v[52:67]
	ds_read_b64_tr_b16 v[84:85], v2 offset:0x600
	ds_read_b64_tr_b16 v[86:87], v2 offset:0xe00
	v_mfma_f32_32x32x16_bf16 v[52:67], v[76:79], v[88:91], v[52:67]
	ds_read_b64_tr_b16 v[88:89], v2 offset:0x1600
	ds_read_b64_tr_b16 v[90:91], v2 offset:0x1e00
	v_mfma_f32_32x32x16_bf16 v[52:67], v[80:83], v[92:95], v[52:67]
	ds_read_b64_tr_b16 v[92:93], v2 offset:0x2600
	ds_read_b64_tr_b16 v[94:95], v2 offset:0x2e00
	v_mfma_f32_32x32x16_bf16 v[52:67], v[68:71], v[96:99], v[52:67]
	ds_read_b64_tr_b16 v[96:97], v2 offset:0x3600
	ds_read_b64_tr_b16 v[98:99], v2 offset:0x3e00
	s_waitcnt lgkmcnt(0)
	v_mfma_f32_32x32x16_bf16 v[4:19], v[72:75], v[84:87], v[4:19]
	v_mfma_f32_32x32x16_bf16 v[4:19], v[76:79], v[88:91], v[4:19]
	v_mfma_f32_32x32x16_bf16 v[4:19], v[80:83], v[92:95], v[4:19]
	v_mfma_f32_32x32x16_bf16 v[4:19], v[68:71], v[96:99], v[4:19]
	s_and_b64 vcc, exec, s[10:11]
	v_mfma_f32_32x32x16_bf16 v[68:83], v[212:215], v[124:127], 0
	v_add_u32_e32 v247, v246, v175
	ds_read_b128 v[212:215], v247 offset:49152
	v_mfma_f32_32x32x16_bf16 v[84:99], v[216:219], v[124:127], 0
	ds_read_b128 v[216:219], v247 offset:57344
	v_mfma_f32_32x32x16_bf16 v[68:83], v[220:223], v[100:103], v[68:83]
	v_add_u32_e32 v247, v246, v176
	ds_read_b128 v[220:223], v247 offset:49152
	v_mfma_f32_32x32x16_bf16 v[84:99], v[224:227], v[100:103], v[84:99]
	ds_read_b128 v[224:227], v247 offset:57344
	v_mfma_f32_32x32x16_bf16 v[68:83], v[228:231], v[104:107], v[68:83]
	v_add_u32_e32 v247, v246, v177
	ds_read_b128 v[228:231], v247 offset:49152
	v_mfma_f32_32x32x16_bf16 v[84:99], v[232:235], v[104:107], v[84:99]
	ds_read_b128 v[232:235], v247 offset:57344
	v_mfma_f32_32x32x16_bf16 v[68:83], v[236:239], v[108:111], v[68:83]
	v_add_u32_e32 v247, v246, v178
	ds_read_b128 v[236:239], v247 offset:49152
	v_mfma_f32_32x32x16_bf16 v[84:99], v[240:243], v[108:111], v[84:99]
	ds_read_b128 v[240:243], v247 offset:57344
	s_waitcnt lgkmcnt(7)
	v_mfma_f32_32x32x16_bf16 v[68:83], v[212:215], v[112:115], v[68:83]
	s_waitcnt lgkmcnt(6)
	v_mfma_f32_32x32x16_bf16 v[84:99], v[216:219], v[112:115], v[84:99]
	s_waitcnt lgkmcnt(5)
	v_mfma_f32_32x32x16_bf16 v[68:83], v[220:223], v[116:119], v[68:83]
	s_waitcnt lgkmcnt(4)
	v_mfma_f32_32x32x16_bf16 v[84:99], v[224:227], v[116:119], v[84:99]
	s_waitcnt lgkmcnt(3)
	v_mfma_f32_32x32x16_bf16 v[68:83], v[228:231], v[120:123], v[68:83]
	s_waitcnt lgkmcnt(2)
	v_mfma_f32_32x32x16_bf16 v[84:99], v[232:235], v[120:123], v[84:99]
	s_waitcnt lgkmcnt(1)
	v_mfma_f32_32x32x16_bf16 v[68:83], v[236:239], v[128:131], v[68:83]
	s_waitcnt lgkmcnt(0)
	v_mfma_f32_32x32x16_bf16 v[84:99], v[240:243], v[128:131], v[84:99]
	s_cbranch_vccnz .LBB0_835
	s_waitcnt vmcnt(0)

; #define LAS __attribute__((address_space(3)))
; __global__ void __launch_bounds__(NTHREADS, 2) fwd(Args args) {
;     extern __shared__ __attribute__((aligned(16))) unsigned char lds_raw[];
;     Frame F; F.lds = (LAS unsigned char*)lds_raw; F.tid = threadIdx.x; F.lane = F.tid & 63; F.wave = __builtin_amdgcn_readfirstlane(F.tid >> 6); F.G = gridDim.x; F.bid = blockIdx.x;
	.amdhsa_kernel _Z3fwd4Args
		.amdhsa_group_segment_fixed_size 0
		.amdhsa_private_segment_fixed_size 0
		.amdhsa_kernarg_size 464
		.amdhsa_user_sgpr_count 2
		.amdhsa_user_sgpr_dispatch_ptr 0
		.amdhsa_user_sgpr_queue_ptr 0
		.amdhsa_user_sgpr_kernarg_segment_ptr 1
		.amdhsa_user_sgpr_dispatch_id 0
		.amdhsa_user_sgpr_kernarg_preload_length 0
		.amdhsa_user_sgpr_kernarg_preload_offset 0
		.amdhsa_user_sgpr_private_segment_size 0
		.amdhsa_uses_dynamic_stack 0
		.amdhsa_enable_private_segment 0
		.amdhsa_system_sgpr_workgroup_id_x 1
		.amdhsa_system_sgpr_workgroup_id_y 0
		.amdhsa_system_sgpr_workgroup_id_z 0
		.amdhsa_system_sgpr_workgroup_info 0
		.amdhsa_system_vgpr_workitem_id 0
		.amdhsa_next_free_vgpr 248
		.amdhsa_next_free_sgpr 100
		.amdhsa_accum_offset 248
		.amdhsa_reserve_vcc 1
		.amdhsa_float_round_mode_32 0
		.amdhsa_float_round_mode_16_64 0
		.amdhsa_float_denorm_mode_32 3
		.amdhsa_float_denorm_mode_16_64 3
		.amdhsa_dx10_clamp 1
		.amdhsa_ieee_mode 1
		.amdhsa_fp16_overflow 0
		.amdhsa_tg_split 0
		.amdhsa_exception_fp_ieee_invalid_op 0
		.amdhsa_exception_fp_denorm_src 0
		.amdhsa_exception_fp_ieee_div_zero 0
		.amdhsa_exception_fp_ieee_overflow 0
		.amdhsa_exception_fp_ieee_underflow 0
		.amdhsa_exception_fp_ieee_inexact 0
		.amdhsa_exception_int_div_zero 0
	.end_amdhsa_kernel

; #define LAS __attribute__((address_space(3)))
; __global__ void __launch_bounds__(NTHREADS, 2) fwd(Args args) {
;     extern __shared__ __attribute__((aligned(16))) unsigned char lds_raw[];
;     Frame F; F.lds = (LAS unsigned char*)lds_raw; F.tid = threadIdx.x; F.lane = F.tid & 63; F.wave = __builtin_amdgcn_readfirstlane(F.tid >> 6); F.G = gridDim.x; F.bid = blockIdx.x;
amdhsa.kernels:
  - .agpr_count:     0
    .args:
      - .offset:         0
        .size:           208
        .value_kind:     by_value
      - .offset:         208
        .size:           4
        .value_kind:     hidden_block_count_x
      - .offset:         212
        .size:           4
        .value_kind:     hidden_block_count_y
      - .offset:         216
        .size:           4
        .value_kind:     hidden_block_count_z
      - .offset:         220
        .size:           2
        .value_kind:     hidden_group_size_x
      - .offset:         222
        .size:           2
        .value_kind:     hidden_group_size_y
      - .offset:         224
        .size:           2
        .value_kind:     hidden_group_size_z
      - .offset:         226
        .size:           2
        .value_kind:     hidden_remainder_x
      - .offset:         228
        .size:           2
        .value_kind:     hidden_remainder_y
      - .offset:         230
        .size:           2
        .value_kind:     hidden_remainder_z
      - .offset:         248
        .size:           8
        .value_kind:     hidden_global_offset_x
      - .offset:         256
        .size:           8
        .value_kind:     hidden_global_offset_y
      - .offset:         264
        .size:           8
        .value_kind:     hidden_global_offset_z
      - .offset:         272
        .size:           2
        .value_kind:     hidden_grid_dims
      - .offset:         328
        .size:           4
        .value_kind:     hidden_dynamic_lds_size
    .group_segment_fixed_size: 0
    .kernarg_segment_align: 8
    .kernarg_segment_size: 464
    .language:       OpenCL C
    .language_version:
      - 2
      - 0
    .max_flat_workgroup_size: 512
    .name:           _Z3fwd4Args
    .private_segment_fixed_size: 0
    .sgpr_count:     106
    .sgpr_spill_count: 70
    .symbol:         _Z3fwd4Args.kd
    .uniform_work_group_size: 1
    .uses_dynamic_stack: false
    .vgpr_count:     248
    .vgpr_spill_count: 0
    .wavefront_size: 64
